# v52 + k_agg2: 8th row of the first gather round requested behind the 4th load instead of after a vmcnt(0) drain; counted waits raised by one
# baseline (speedup 1.0000x reference)
.LBB3_2:
	s_or_b64 exec, exec, s[2:3]
	v_mbcnt_lo_u32_b32 v10, -1, 0
	v_mbcnt_hi_u32_b32 v27, -1, v10
	s_waitcnt vmcnt(1)
	v_cmp_gt_i32_e64 s[2:3], v45, v41
	v_and_or_b32 v9, v27, 64, v9
	v_lshlrev_b32_e32 v47, 2, v9
	s_waitcnt vmcnt(0)
	v_cndmask_b32_e64 v8, v24, v8, s[2:3]
	ds_bpermute_b32 v10, v47, v8
	ds_bpermute_b32 v14, v47, v8 offset:16
	ds_bpermute_b32 v20, v47, v8 offset:48
	v_cndmask_b32_e64 v49, 0, 1.0, s[2:3]
	ds_bpermute_b32 v40, v47, v49
	s_waitcnt lgkmcnt(3)
	v_ashrrev_i32_e32 v11, 31, v10
	v_lshlrev_b64 v[10:11], 7, v[10:11]
	v_lshl_add_u64 v[10:11], v[30:31], 0, v[10:11]
	global_load_dwordx4 v[10:13], v[10:11], off
	s_waitcnt lgkmcnt(2)
	v_ashrrev_i32_e32 v15, 31, v14
	v_lshlrev_b64 v[14:15], 7, v[14:15]
	v_lshl_add_u64 v[14:15], v[30:31], 0, v[14:15]
	global_load_dwordx4 v[14:17], v[14:15], off
	s_waitcnt lgkmcnt(1)
	v_ashrrev_i32_e32 v21, 31, v20
	v_lshlrev_b64 v[22:23], 7, v[20:21]
	v_lshl_add_u64 v[22:23], v[30:31], 0, v[22:23]
	global_load_dwordx4 v[32:35], v[22:23], off
	ds_bpermute_b32 v18, v47, v8 offset:32
	ds_bpermute_b32 v42, v47, v49 offset:16
	ds_bpermute_b32 v44, v47, v49 offset:64
	v_cmp_lt_i32_e64 s[2:3], 32, v45
	s_waitcnt lgkmcnt(2)
	v_ashrrev_i32_e32 v19, 31, v18
	v_lshlrev_b64 v[18:19], 7, v[18:19]
	v_lshl_add_u64 v[18:19], v[30:31], 0, v[18:19]
	global_load_dwordx4 v[18:21], v[18:19], off
	ds_bpermute_b32 v52, v47, v8 offset:112
	s_waitcnt lgkmcnt(0)
	v_ashrrev_i32_e32 v53, 31, v52
	v_lshlrev_b64 v[52:53], 7, v[52:53]
	v_lshl_add_u64 v[52:53], v[30:31], 0, v[52:53]
	global_load_dwordx4 v[52:55], v[52:53], off
	s_waitcnt vmcnt(4)
	v_fma_mix_f32 v6, v40, v10, v6 op_sel_hi:[0,1,0]
	v_fma_mix_f32 v7, v40, v10, v7 op_sel:[0,1,0] op_sel_hi:[0,1,0]
	ds_bpermute_b32 v22, v47, v8 offset:64
	v_fma_mix_f32 v10, v40, v11, v4 op_sel_hi:[0,1,0]
	v_fma_mix_f32 v11, v40, v11, v5 op_sel:[0,1,0] op_sel_hi:[0,1,0]
	ds_bpermute_b32 v4, v47, v8 offset:80
	s_waitcnt lgkmcnt(1)
	v_ashrrev_i32_e32 v23, 31, v22
	v_fma_mix_f32 v36, v40, v12, v2 op_sel_hi:[0,1,0]
	v_fma_mix_f32 v37, v40, v12, v3 op_sel:[0,1,0] op_sel_hi:[0,1,0]
	v_lshlrev_b64 v[2:3], 7, v[22:23]
	v_lshl_add_u64 v[2:3], v[30:31], 0, v[2:3]
	s_waitcnt vmcnt(3)
	v_fma_mix_f32 v22, v40, v13, v0 op_sel_hi:[0,1,0]
	v_fma_mix_f32 v23, v40, v13, v1 op_sel:[0,1,0] op_sel_hi:[0,1,0]
	global_load_dwordx4 v[0:3], v[2:3], off
	ds_bpermute_b32 v12, v47, v8 offset:96
	s_waitcnt lgkmcnt(1)
	v_ashrrev_i32_e32 v5, 31, v4
	v_lshlrev_b64 v[4:5], 7, v[4:5]
	v_lshl_add_u64 v[4:5], v[30:31], 0, v[4:5]
	v_fma_mix_f32 v38, v42, v14, v6 op_sel_hi:[0,1,0]
	v_fma_mix_f32 v39, v42, v14, v7 op_sel:[0,1,0] op_sel_hi:[0,1,0]
	global_load_dwordx4 v[4:7], v[4:5], off
	s_waitcnt lgkmcnt(0)
	v_ashrrev_i32_e32 v13, 31, v12
	v_lshlrev_b64 v[12:13], 7, v[12:13]
	v_lshl_add_u64 v[12:13], v[30:31], 0, v[12:13]
	v_fma_mix_f32 v60, v42, v15, v10 op_sel_hi:[0,1,0]
	v_fma_mix_f32 v61, v42, v15, v11 op_sel:[0,1,0] op_sel_hi:[0,1,0]
	global_load_dwordx4 v[10:13], v[12:13], off
	ds_bpermute_b32 v40, v47, v49 offset:32
	s_waitcnt vmcnt(4)
	v_fma_mix_f32 v50, v42, v16, v36 op_sel_hi:[0,1,0]
	v_fma_mix_f32 v51, v42, v16, v37 op_sel:[0,1,0] op_sel_hi:[0,1,0]
	v_fma_mix_f32 v22, v42, v17, v22 op_sel_hi:[0,1,0]
	v_fma_mix_f32 v23, v42, v17, v23 op_sel:[0,1,0] op_sel_hi:[0,1,0]
	ds_bpermute_b32 v42, v47, v49 offset:48
	s_waitcnt lgkmcnt(1)
	v_fma_mix_f32 v14, v40, v18, v38 op_sel_hi:[0,1,0]
	v_fma_mix_f32 v15, v40, v18, v39 op_sel:[0,1,0] op_sel_hi:[0,1,0]
	s_waitcnt lgkmcnt(0)
	v_fma_mix_f32 v14, v42, v32, v14 op_sel_hi:[0,1,0]
	v_fma_mix_f32 v15, v42, v32, v15 op_sel:[0,1,0] op_sel_hi:[0,1,0]
	v_fma_mix_f32 v18, v40, v19, v60 op_sel_hi:[0,1,0]
	v_fma_mix_f32 v19, v40, v19, v61 op_sel:[0,1,0] op_sel_hi:[0,1,0]
	v_fma_mix_f32 v18, v42, v33, v18 op_sel_hi:[0,1,0]
	v_fma_mix_f32 v19, v42, v33, v19 op_sel:[0,1,0] op_sel_hi:[0,1,0]
	s_waitcnt vmcnt(2)
	v_cvt_f32_f16_e32 v16, v0
	v_cvt_f32_f16_sdwa v17, v0 dst_sel:DWORD dst_unused:UNUSED_PAD src0_sel:WORD_1
	ds_bpermute_b32 v0, v47, v49 offset:80
	v_pk_fma_f32 v[14:15], v[44:45], v[16:17], v[14:15] op_sel_hi:[0,1,1]
	s_waitcnt vmcnt(1)
	v_cvt_f32_f16_e32 v16, v4
	v_cvt_f32_f16_sdwa v17, v4 dst_sel:DWORD dst_unused:UNUSED_PAD src0_sel:WORD_1
	ds_bpermute_b32 v4, v47, v49 offset:96
	v_fma_mix_f32 v18, v44, v1, v18 op_sel_hi:[0,1,0]
	v_fma_mix_f32 v19, v44, v1, v19 op_sel:[0,1,0] op_sel_hi:[0,1,0]
	s_waitcnt lgkmcnt(1)
	v_pk_fma_f32 v[14:15], v[0:1], v[16:17], v[14:15] op_sel_hi:[0,1,1]
	s_waitcnt vmcnt(0)
	v_cvt_f32_f16_e32 v16, v10
	v_cvt_f32_f16_sdwa v17, v10 dst_sel:DWORD dst_unused:UNUSED_PAD src0_sel:WORD_1
	ds_bpermute_b32 v10, v47, v49 offset:112
	s_waitcnt lgkmcnt(1)
	v_pk_fma_f32 v[36:37], v[4:5], v[16:17], v[14:15] op_sel_hi:[0,1,1]
	v_fma_mix_f32 v18, v0, v5, v18 op_sel_hi:[0,1,0]
	v_fma_mix_f32 v19, v0, v5, v19 op_sel:[0,1,0] op_sel_hi:[0,1,0]
	s_waitcnt lgkmcnt(0)
	v_fma_mix_f32 v18, v4, v11, v18 op_sel_hi:[0,1,0]
	v_fma_mix_f32 v19, v4, v11, v19 op_sel:[0,1,0] op_sel_hi:[0,1,0]
	s_waitcnt vmcnt(0)
	v_fma_mix_f32 v36, v10, v52, v36 op_sel_hi:[0,1,0]
	v_fma_mix_f32 v37, v10, v52, v37 op_sel:[0,1,0] op_sel_hi:[0,1,0]
	v_fma_mix_f32 v38, v10, v53, v18 op_sel_hi:[0,1,0]
	v_fma_mix_f32 v39, v10, v53, v19 op_sel:[0,1,0] op_sel_hi:[0,1,0]
	v_cvt_f32_f16_e32 v18, v2
	v_cvt_f32_f16_sdwa v19, v2 dst_sel:DWORD dst_unused:UNUSED_PAD src0_sel:WORD_1
	v_fma_mix_f32 v14, v40, v20, v50 op_sel_hi:[0,1,0]
	v_fma_mix_f32 v15, v40, v20, v51 op_sel:[0,1,0] op_sel_hi:[0,1,0]
	v_fma_mix_f32 v14, v42, v34, v14 op_sel_hi:[0,1,0]
	v_fma_mix_f32 v15, v42, v34, v15 op_sel:[0,1,0] op_sel_hi:[0,1,0]
	v_cvt_f32_f16_e32 v2, v3
	v_pk_fma_f32 v[14:15], v[44:45], v[18:19], v[14:15] op_sel_hi:[0,1,1]
	v_cvt_f32_f16_e32 v18, v6
	v_cvt_f32_f16_sdwa v19, v6 dst_sel:DWORD dst_unused:UNUSED_PAD src0_sel:WORD_1
	v_cvt_f32_f16_sdwa v3, v3 dst_sel:DWORD dst_unused:UNUSED_PAD src0_sel:WORD_1
	v_cvt_f32_f16_e32 v6, v7
	v_cvt_f32_f16_sdwa v7, v7 dst_sel:DWORD dst_unused:UNUSED_PAD src0_sel:WORD_1
	v_pk_fma_f32 v[14:15], v[0:1], v[18:19], v[14:15] op_sel_hi:[0,1,1]
	v_cvt_f32_f16_e32 v18, v12
	v_cvt_f32_f16_sdwa v19, v12 dst_sel:DWORD dst_unused:UNUSED_PAD src0_sel:WORD_1
	v_cvt_f32_f16_e32 v12, v13
	v_cvt_f32_f16_sdwa v13, v13 dst_sel:DWORD dst_unused:UNUSED_PAD src0_sel:WORD_1
	v_pk_fma_f32 v[14:15], v[4:5], v[18:19], v[14:15] op_sel_hi:[0,1,1]
	v_cvt_f32_f16_e32 v18, v54
	v_cvt_f32_f16_sdwa v19, v54 dst_sel:DWORD dst_unused:UNUSED_PAD src0_sel:WORD_1
	v_cvt_f32_f16_e32 v16, v55
	v_cvt_f32_f16_sdwa v17, v55 dst_sel:DWORD dst_unused:UNUSED_PAD src0_sel:WORD_1
	v_pk_fma_f32 v[32:33], v[10:11], v[18:19], v[14:15] op_sel_hi:[0,1,1]
	v_fma_mix_f32 v14, v40, v21, v22 op_sel_hi:[0,1,0]
	v_fma_mix_f32 v15, v40, v21, v23 op_sel:[0,1,0] op_sel_hi:[0,1,0]
	v_fma_mix_f32 v14, v42, v35, v14 op_sel_hi:[0,1,0]
	v_fma_mix_f32 v15, v42, v35, v15 op_sel:[0,1,0] op_sel_hi:[0,1,0]
	v_pk_fma_f32 v[2:3], v[44:45], v[2:3], v[14:15] op_sel_hi:[0,1,1]
	v_pk_fma_f32 v[0:1], v[0:1], v[6:7], v[2:3] op_sel_hi:[0,1,1]
	v_pk_fma_f32 v[0:1], v[4:5], v[12:13], v[0:1] op_sel_hi:[0,1,1]
	v_pk_fma_f32 v[34:35], v[10:11], v[16:17], v[0:1] op_sel_hi:[0,1,1]
	s_and_saveexec_b64 s[6:7], s[2:3]
	s_cbranch_execz .LBB3_4
	ds_bpermute_b32 v0, v47, v8 offset:128
	ds_bpermute_b32 v2, v47, v8 offset:144
	ds_bpermute_b32 v4, v47, v8 offset:176
	ds_bpermute_b32 v6, v47, v8 offset:208
	ds_bpermute_b32 v10, v47, v8 offset:224
	s_waitcnt lgkmcnt(4)
	v_ashrrev_i32_e32 v1, 31, v0
	s_waitcnt lgkmcnt(3)
	v_ashrrev_i32_e32 v3, 31, v2
	v_lshlrev_b64 v[0:1], 7, v[0:1]
	v_lshlrev_b64 v[2:3], 7, v[2:3]
	v_lshl_add_u64 v[0:1], v[30:31], 0, v[0:1]
	v_lshl_add_u64 v[2:3], v[30:31], 0, v[2:3]
	global_load_dwordx4 v[52:55], v[0:1], off
	global_load_dwordx4 v[58:61], v[2:3], off
	ds_bpermute_b32 v0, v47, v8 offset:160
	ds_bpermute_b32 v2, v47, v8 offset:192
	s_waitcnt lgkmcnt(4)
	v_ashrrev_i32_e32 v5, 31, v4
	s_waitcnt lgkmcnt(3)
	v_ashrrev_i32_e32 v7, 31, v6
	s_waitcnt lgkmcnt(2)
	v_ashrrev_i32_e32 v11, 31, v10
	s_waitcnt lgkmcnt(1)
	v_ashrrev_i32_e32 v1, 31, v0
	v_lshlrev_b64 v[0:1], 7, v[0:1]
	v_lshl_add_u64 v[0:1], v[30:31], 0, v[0:1]
	global_load_dwordx4 v[16:19], v[0:1], off
	v_lshlrev_b64 v[0:1], 7, v[4:5]
	s_waitcnt lgkmcnt(0)
	v_ashrrev_i32_e32 v3, 31, v2
	v_lshl_add_u64 v[0:1], v[30:31], 0, v[0:1]
	global_load_dwordx4 v[20:23], v[0:1], off
	v_lshlrev_b64 v[0:1], 7, v[2:3]
	v_lshl_add_u64 v[0:1], v[30:31], 0, v[0:1]
	global_load_dwordx4 v[12:15], v[0:1], off
	v_lshlrev_b64 v[0:1], 7, v[6:7]
	v_lshl_add_u64 v[0:1], v[30:31], 0, v[0:1]
	global_load_dwordx4 v[4:7], v[0:1], off
	ds_bpermute_b32 v0, v47, v8 offset:240
	v_lshlrev_b64 v[2:3], 7, v[10:11]
	v_lshl_add_u64 v[2:3], v[30:31], 0, v[2:3]
	global_load_dwordx4 v[8:11], v[2:3], off
	ds_bpermute_b32 v46, v47, v49 offset:128
	s_waitcnt lgkmcnt(1)
	v_ashrrev_i32_e32 v1, 31, v0
	v_lshlrev_b64 v[0:1], 7, v[0:1]
	v_lshl_add_u64 v[0:1], v[30:31], 0, v[0:1]
	global_load_dwordx4 v[0:3], v[0:1], off
	ds_bpermute_b32 v48, v47, v49 offset:144
	ds_bpermute_b32 v50, v47, v49 offset:160
	ds_bpermute_b32 v44, v47, v49 offset:176
	ds_bpermute_b32 v40, v47, v49 offset:192
	ds_bpermute_b32 v42, v47, v49 offset:208
	s_waitcnt vmcnt(7)
	s_waitcnt vmcnt(6)
	s_waitcnt vmcnt(5)
	s_waitcnt lgkmcnt(5)
	v_fma_mix_f32 v36, v46, v52, v36 op_sel_hi:[0,1,0]
	v_fma_mix_f32 v37, v46, v52, v37 op_sel:[0,1,0] op_sel_hi:[0,1,0]
	s_waitcnt vmcnt(4)
	v_fma_mix_f32 v38, v46, v53, v38 op_sel_hi:[0,1,0]
	v_fma_mix_f32 v39, v46, v53, v39 op_sel:[0,1,0] op_sel_hi:[0,1,0]
	s_waitcnt vmcnt(3)
	v_cvt_f32_f16_e32 v56, v54
	v_cvt_f32_f16_sdwa v57, v54 dst_sel:DWORD dst_unused:UNUSED_PAD src0_sel:WORD_1
	ds_bpermute_b32 v54, v47, v49 offset:224
	s_waitcnt lgkmcnt(5)
	v_fma_mix_f32 v36, v48, v58, v36 op_sel_hi:[0,1,0]
	v_fma_mix_f32 v37, v48, v58, v37 op_sel:[0,1,0] op_sel_hi:[0,1,0]
	s_waitcnt vmcnt(2)
	v_fma_mix_f32 v38, v48, v59, v38 op_sel_hi:[0,1,0]
	v_fma_mix_f32 v39, v48, v59, v39 op_sel:[0,1,0] op_sel_hi:[0,1,0]
	ds_bpermute_b32 v52, v47, v49 offset:240
	s_waitcnt lgkmcnt(5)
	v_fma_mix_f32 v36, v50, v16, v36 op_sel_hi:[0,1,0]
	v_fma_mix_f32 v37, v50, v16, v37 op_sel:[0,1,0] op_sel_hi:[0,1,0]
	s_waitcnt vmcnt(1)
	v_fma_mix_f32 v16, v50, v17, v38 op_sel_hi:[0,1,0]
	v_fma_mix_f32 v17, v50, v17, v39 op_sel:[0,1,0] op_sel_hi:[0,1,0]
	s_waitcnt lgkmcnt(4)
	v_fma_mix_f32 v36, v44, v20, v36 op_sel_hi:[0,1,0]
	v_fma_mix_f32 v37, v44, v20, v37 op_sel:[0,1,0] op_sel_hi:[0,1,0]
	s_waitcnt vmcnt(0)
	v_fma_mix_f32 v16, v44, v21, v16 op_sel_hi:[0,1,0]
	v_fma_mix_f32 v17, v44, v21, v17 op_sel:[0,1,0] op_sel_hi:[0,1,0]
	s_waitcnt lgkmcnt(3)
	v_fma_mix_f32 v20, v40, v12, v36 op_sel_hi:[0,1,0]
	v_fma_mix_f32 v21, v40, v12, v37 op_sel:[0,1,0] op_sel_hi:[0,1,0]
	v_fma_mix_f32 v12, v40, v13, v16 op_sel_hi:[0,1,0]
	v_fma_mix_f32 v13, v40, v13, v17 op_sel:[0,1,0] op_sel_hi:[0,1,0]
	s_waitcnt lgkmcnt(2)
	v_fma_mix_f32 v20, v42, v4, v20 op_sel_hi:[0,1,0]
	v_fma_mix_f32 v21, v42, v4, v21 op_sel:[0,1,0] op_sel_hi:[0,1,0]
	v_fma_mix_f32 v4, v42, v5, v12 op_sel_hi:[0,1,0]
	v_fma_mix_f32 v5, v42, v5, v13 op_sel:[0,1,0] op_sel_hi:[0,1,0]
	s_waitcnt lgkmcnt(1)
	v_fma_mix_f32 v20, v54, v8, v20 op_sel_hi:[0,1,0]
	v_fma_mix_f32 v21, v54, v8, v21 op_sel:[0,1,0] op_sel_hi:[0,1,0]
	v_fma_mix_f32 v4, v54, v9, v4 op_sel_hi:[0,1,0]
	v_fma_mix_f32 v5, v54, v9, v5 op_sel:[0,1,0] op_sel_hi:[0,1,0]
	s_waitcnt lgkmcnt(0)
	v_fma_mix_f32 v36, v52, v0, v20 op_sel_hi:[0,1,0]
	v_fma_mix_f32 v37, v52, v0, v21 op_sel:[0,1,0] op_sel_hi:[0,1,0]
	v_fma_mix_f32 v38, v52, v1, v4 op_sel_hi:[0,1,0]
	v_fma_mix_f32 v39, v52, v1, v5 op_sel:[0,1,0] op_sel_hi:[0,1,0]
	v_pk_fma_f32 v[8:9], v[46:47], v[56:57], v[32:33] op_sel_hi:[0,1,1]
	v_fma_mix_f32 v8, v48, v60, v8 op_sel_hi:[0,1,0]
	v_fma_mix_f32 v9, v48, v60, v9 op_sel:[0,1,0] op_sel_hi:[0,1,0]
	v_fma_mix_f32 v0, v50, v18, v8 op_sel_hi:[0,1,0]
	v_fma_mix_f32 v1, v50, v18, v9 op_sel:[0,1,0] op_sel_hi:[0,1,0]
	v_fma_mix_f32 v0, v44, v22, v0 op_sel_hi:[0,1,0]
	v_fma_mix_f32 v1, v44, v22, v1 op_sel:[0,1,0] op_sel_hi:[0,1,0]
	v_fma_mix_f32 v0, v40, v14, v0 op_sel_hi:[0,1,0]
	v_fma_mix_f32 v1, v40, v14, v1 op_sel:[0,1,0] op_sel_hi:[0,1,0]
	v_fma_mix_f32 v0, v42, v6, v0 op_sel_hi:[0,1,0]
	v_fma_mix_f32 v1, v42, v6, v1 op_sel:[0,1,0] op_sel_hi:[0,1,0]
	v_fma_mix_f32 v0, v54, v10, v0 op_sel_hi:[0,1,0]
	v_fma_mix_f32 v1, v54, v10, v1 op_sel:[0,1,0] op_sel_hi:[0,1,0]
	v_fma_mix_f32 v32, v52, v2, v0 op_sel_hi:[0,1,0]
	v_fma_mix_f32 v33, v52, v2, v1 op_sel:[0,1,0] op_sel_hi:[0,1,0]
	v_fma_mix_f32 v8, v46, v55, v34 op_sel_hi:[0,1,0]
	v_fma_mix_f32 v9, v46, v55, v35 op_sel:[0,1,0] op_sel_hi:[0,1,0]
	v_fma_mix_f32 v8, v48, v61, v8 op_sel_hi:[0,1,0]
	v_fma_mix_f32 v9, v48, v61, v9 op_sel:[0,1,0] op_sel_hi:[0,1,0]
	v_fma_mix_f32 v0, v50, v19, v8 op_sel_hi:[0,1,0]
	v_fma_mix_f32 v1, v50, v19, v9 op_sel:[0,1,0] op_sel_hi:[0,1,0]
	v_fma_mix_f32 v0, v44, v23, v0 op_sel_hi:[0,1,0]
	v_fma_mix_f32 v1, v44, v23, v1 op_sel:[0,1,0] op_sel_hi:[0,1,0]
	v_fma_mix_f32 v0, v40, v15, v0 op_sel_hi:[0,1,0]
	v_fma_mix_f32 v1, v40, v15, v1 op_sel:[0,1,0] op_sel_hi:[0,1,0]
	v_fma_mix_f32 v0, v42, v7, v0 op_sel_hi:[0,1,0]
	v_fma_mix_f32 v1, v42, v7, v1 op_sel:[0,1,0] op_sel_hi:[0,1,0]
	v_fma_mix_f32 v0, v54, v11, v0 op_sel_hi:[0,1,0]
	v_fma_mix_f32 v1, v54, v11, v1 op_sel:[0,1,0] op_sel_hi:[0,1,0]
	v_fma_mix_f32 v34, v52, v3, v0 op_sel_hi:[0,1,0]
	v_fma_mix_f32 v35, v52, v3, v1 op_sel:[0,1,0] op_sel_hi:[0,1,0]
